# MoE gate/up: six of the eight per-row scale loads of the epilogue issued in the last K iteration beside the bias prefetch; last-iteration DMA waits counted for the extra loads
# baseline (speedup 1.0000x reference)
; #define PG8_STAGE_A(bufoff, soff, voff) do { _Pragma("unroll") for (int _i = 0; _i < 2; ++_i) \
;         __builtin_amdgcn_raw_ptr_buffer_load_lds(rsA, (LAS void*)(lds + (bufoff) + ldsw + _i * 8192), 16, (voff)[_i], (soff), 0, 0); } while (0)
; #define PG8_STAGE_B(bufoff, soff) do { _Pragma("unroll") for (int _i = 0; _i < 2; ++_i) \
;         __builtin_amdgcn_raw_ptr_buffer_load_lds(rsB, (LAS void*)(lds + (bufoff) + ldsw + _i * 8192), 16, voffB[_i], (soff), 0, 0); } while (0)
; #define PG8_LDA(dst, b, h) do { _Pragma("unroll") for (int m = 0; m < 4; ++m) dst[m] = PG8_LD8(lds + PG8_SA(b, h) + aoff + m * 2048); } while (0)
; #define PG8_LDB(dst, b, h) do { _Pragma("unroll") for (int n = 0; n < 2; ++n) dst[n] = PG8_LD8(lds + PG8_SB(b, h) + boff + n * 2048); } while (0)
; #define PG8_WAIT_V(n) asm volatile("s_waitcnt vmcnt(" #n ")" ::: "memory")
; #define PG8_WAIT_L(n) asm volatile("s_waitcnt lgkmcnt(" #n ")" ::: "memory")
; #define PG8_BAR __builtin_amdgcn_s_barrier()
; #define PG8_SCHED __builtin_amdgcn_sched_barrier(0)
; template <class Epi, class Sched, bool GATHER, bool ALIGN_EPI, bool SP2, bool FP8>
; __device__ __forceinline__ void gemm_phase(LAS unsigned char* lds, const Gemm g, const Sched& S, const Epi& E) {
;     ...
;             if (last) pre = E.prefetch(cur, wr, wc, fr, fq);
;     ...
;             PG8_LDB(B0, 0, 0); PG8_LDB(B1, 0, 1); PG8_SCHED; PG8_LDA(At, 0, 0); PG8_STAGE_A(PG8_SA(1, 1), a1, vA1);
;             PG8_WAIT_V(8); PG8_WAIT_L(0); PG8_BAR; PG8_MMA(0, 0, At, B0); PG8_MMA(0, 1, At, B1); PG8_BAR; PG8_SCHED;
;             PG8_LDA(At, 0, 1); PG8_STAGE_B(PG8_SB(0, 0), b2); PG8_STAGE_B(PG8_SB(0, 1), b2 + hstep); PG8_STAGE_A(PG8_SA(0, 0), a2, va20);
;             PG8_WAIT_V(8); PG8_WAIT_L(0); PG8_BAR; PG8_MMA(1, 0, At, B0); PG8_MMA(1, 1, At, B1); PG8_BAR; PG8_SCHED;
.LBB0_931:
	s_and_b64 s[8:9], s[2:3], exec
	s_cselect_b32 s8, 0, s6
	s_add_i32 s9, s80, s6
	s_or_b32 s7, s8, 0x80
	s_and_b64 s[2:3], s[2:3], exec
	s_cselect_b32 s2, s25, s9
	s_add_i32 s3, s6, 0xffffff80
	s_mov_b32 s66, s62
	s_mov_b32 s67, s63
	v_add_u32_e32 v14, 0x10000, v176
	ds_read_b128 v[2:5], v14
	ds_read_b128 v[6:9], v14 offset:1024
	ds_read_b128 v[10:13], v14 offset:2048
	ds_read_b128 v[14:17], v14 offset:3072
	v_add_u32_e32 v191, 0x14000, v176
	ds_read_b128 v[224:227], v191
	ds_read_b128 v[228:231], v191 offset:1024
	ds_read_b128 v[232:235], v191 offset:2048
	ds_read_b128 v[236:239], v191 offset:3072
	ds_read_b128 v[192:195], v177
	ds_read_b128 v[196:199], v177 offset:1024
	ds_read_b128 v[200:203], v177 offset:2048
	ds_read_b128 v[204:207], v177 offset:3072
	ds_read_b128 v[208:211], v177 offset:4096
	ds_read_b128 v[212:215], v177 offset:5120
	ds_read_b128 v[216:219], v177 offset:6144
	ds_read_b128 v[220:223], v177 offset:7168
	s_mov_b32 m0, s51
	s_nop 0
	buffer_load_dwordx4 v184, s[60:63], s3 offen lds
	s_mov_b32 m0, s52
	s_nop 0
	buffer_load_dwordx4 v186, s[60:63], s3 offen lds
	s_cmp_eq_u32 s5, 12
	s_cbranch_scc1 .Lp5w0_last
	s_waitcnt vmcnt(8)
	s_branch .Lp5w0_join
.Lp5w0_last:
	s_waitcnt vmcnt(18)
.Lp5w0_join:
	s_waitcnt lgkmcnt(0)
	s_barrier
	s_setprio 1
	v_mfma_f32_16x16x128_f8f6f4 v[158:161], v[2:9], v[192:199], v[158:161]
	v_mfma_f32_16x16x128_f8f6f4 v[154:157], v[10:17], v[192:199], v[154:157]
	v_mfma_f32_16x16x128_f8f6f4 v[142:145], v[2:9], v[200:207], v[142:145]
	v_mfma_f32_16x16x128_f8f6f4 v[138:141], v[10:17], v[200:207], v[138:141]
	v_mfma_f32_16x16x128_f8f6f4 v[126:129], v[2:9], v[208:215], v[126:129]
	v_mfma_f32_16x16x128_f8f6f4 v[122:125], v[10:17], v[208:215], v[122:125]
	v_mfma_f32_16x16x128_f8f6f4 v[110:113], v[2:9], v[216:223], v[110:113]
	v_mfma_f32_16x16x128_f8f6f4 v[106:109], v[10:17], v[216:223], v[106:109]
	v_mfma_f32_16x16x128_f8f6f4 v[150:153], v[224:231], v[192:199], v[150:153]
	v_mfma_f32_16x16x128_f8f6f4 v[146:149], v[232:239], v[192:199], v[146:149]
	v_mfma_f32_16x16x128_f8f6f4 v[134:137], v[224:231], v[200:207], v[134:137]
	v_mfma_f32_16x16x128_f8f6f4 v[130:133], v[232:239], v[200:207], v[130:133]
	v_mfma_f32_16x16x128_f8f6f4 v[118:121], v[224:231], v[208:215], v[118:121]
	v_mfma_f32_16x16x128_f8f6f4 v[114:117], v[232:239], v[208:215], v[114:117]
	v_mfma_f32_16x16x128_f8f6f4 v[102:105], v[224:231], v[216:223], v[102:105]
	v_mfma_f32_16x16x128_f8f6f4 v[98:101], v[232:239], v[216:223], v[98:101]
	s_setprio 0
	s_barrier
	ds_read_b128 v[192:195], v177 offset:16384
	ds_read_b128 v[196:199], v177 offset:17408
	ds_read_b128 v[200:203], v177 offset:18432
	ds_read_b128 v[204:207], v177 offset:19456
	ds_read_b128 v[208:211], v177 offset:20480
	ds_read_b128 v[212:215], v177 offset:21504
	ds_read_b128 v[216:219], v177 offset:22528
	ds_read_b128 v[220:223], v177 offset:23552
	s_mov_b32 m0, s37
	s_nop 0
	buffer_load_dwordx4 v173, s[64:67], s2 offen lds
	s_mov_b32 m0, s38
	s_nop 0
	buffer_load_dwordx4 v174, s[64:67], s2 offen lds
	s_add_i32 s3, s2, 0x40000
	s_mov_b32 m0, s40
	s_nop 0
	buffer_load_dwordx4 v173, s[64:67], s3 offen lds
	s_mov_b32 m0, s41
	s_nop 0
	buffer_load_dwordx4 v174, s[64:67], s3 offen lds
	s_mov_b32 m0, s36
	s_nop 0
	buffer_load_dwordx4 v187, s[60:63], s8 offen lds
	s_mov_b32 m0, s39
	s_nop 0
	buffer_load_dwordx4 v188, s[60:63], s8 offen lds
	s_cmp_eq_u32 s5, 12
	s_cbranch_scc1 .Lp5w1_last
	s_waitcnt vmcnt(8)
	s_branch .Lp5w1_join

; #define PG8_STAGE_A(bufoff, soff, voff) do { _Pragma("unroll") for (int _i = 0; _i < 2; ++_i) \
;         __builtin_amdgcn_raw_ptr_buffer_load_lds(rsA, (LAS void*)(lds + (bufoff) + ldsw + _i * 8192), 16, (voff)[_i], (soff), 0, 0); } while (0)
; #define PG8_STAGE_B(bufoff, soff) do { _Pragma("unroll") for (int _i = 0; _i < 2; ++_i) \
;         __builtin_amdgcn_raw_ptr_buffer_load_lds(rsB, (LAS void*)(lds + (bufoff) + ldsw + _i * 8192), 16, voffB[_i], (soff), 0, 0); } while (0)
; #define PG8_LDA(dst, b, h) do { _Pragma("unroll") for (int m = 0; m < 4; ++m) dst[m] = PG8_LD8(lds + PG8_SA(b, h) + aoff + m * 2048); } while (0)
; #define PG8_LDB(dst, b, h) do { _Pragma("unroll") for (int n = 0; n < 2; ++n) dst[n] = PG8_LD8(lds + PG8_SB(b, h) + boff + n * 2048); } while (0)
; #define PG8_WAIT_V(n) asm volatile("s_waitcnt vmcnt(" #n ")" ::: "memory")
; #define PG8_WAIT_L(n) asm volatile("s_waitcnt lgkmcnt(" #n ")" ::: "memory")
; #define PG8_BAR __builtin_amdgcn_s_barrier()
; #define PG8_SCHED __builtin_amdgcn_sched_barrier(0)
; template <class Epi, class Sched, bool GATHER, bool ALIGN_EPI, bool SP2, bool FP8>
; __device__ __forceinline__ void gemm_phase(LAS unsigned char* lds, const Gemm g, const Sched& S, const Epi& E) {
;     ...
;             PG8_WAIT_V(8); PG8_WAIT_L(0); PG8_BAR; PG8_MMA(1, 0, At, B0); PG8_MMA(1, 1, At, B1); PG8_BAR; PG8_SCHED;
;             PG8_LDB(B0, 1, 0); PG8_LDB(B1, 1, 1); PG8_SCHED; PG8_LDA(At, 1, 0); PG8_STAGE_A(PG8_SA(0, 1), a2, va21);
;             PG8_WAIT_V(8); PG8_WAIT_L(0); PG8_BAR; PG8_MMA(0, 0, At, B0); PG8_MMA(0, 1, At, B1); PG8_BAR; PG8_SCHED;
;             PG8_LDA(At, 1, 1); PG8_STAGE_B(PG8_SB(1, 0), b3); PG8_STAGE_B(PG8_SB(1, 1), b3 + hstep); PG8_STAGE_A(PG8_SA(1, 0), a3, va20);
;             PG8_WAIT_V(8); PG8_WAIT_L(0); PG8_BAR; PG8_MMA(1, 0, At, B0); PG8_MMA(1, 1, At, B1); PG8_BAR; PG8_SCHED;
.Lp5w1_join:
	s_waitcnt lgkmcnt(0)
	s_barrier
	s_setprio 1
	v_mfma_f32_16x16x128_f8f6f4 v[94:97], v[2:9], v[192:199], v[94:97]
	v_mfma_f32_16x16x128_f8f6f4 v[90:93], v[10:17], v[192:199], v[90:93]
	v_mfma_f32_16x16x128_f8f6f4 v[78:81], v[2:9], v[200:207], v[78:81]
	v_mfma_f32_16x16x128_f8f6f4 v[74:77], v[10:17], v[200:207], v[74:77]
	v_mfma_f32_16x16x128_f8f6f4 v[62:65], v[2:9], v[208:215], v[62:65]
	v_mfma_f32_16x16x128_f8f6f4 v[58:61], v[10:17], v[208:215], v[58:61]
	v_mfma_f32_16x16x128_f8f6f4 v[46:49], v[2:9], v[216:223], v[46:49]
	v_mfma_f32_16x16x128_f8f6f4 v[42:45], v[10:17], v[216:223], v[42:45]
	v_mfma_f32_16x16x128_f8f6f4 v[86:89], v[224:231], v[192:199], v[86:89]
	v_mfma_f32_16x16x128_f8f6f4 v[82:85], v[232:239], v[192:199], v[82:85]
	v_mfma_f32_16x16x128_f8f6f4 v[70:73], v[224:231], v[200:207], v[70:73]
	v_mfma_f32_16x16x128_f8f6f4 v[66:69], v[232:239], v[200:207], v[66:69]
	v_mfma_f32_16x16x128_f8f6f4 v[54:57], v[224:231], v[208:215], v[54:57]
	v_mfma_f32_16x16x128_f8f6f4 v[50:53], v[232:239], v[208:215], v[50:53]
	v_mfma_f32_16x16x128_f8f6f4 v[38:41], v[224:231], v[216:223], v[38:41]
	v_mfma_f32_16x16x128_f8f6f4 v[34:37], v[232:239], v[216:223], v[34:37]
	s_setprio 0
	s_barrier
	v_add_u32_e32 v14, 0x18000, v176
	ds_read_b128 v[2:5], v14
	ds_read_b128 v[6:9], v14 offset:1024
	ds_read_b128 v[10:13], v14 offset:2048
	ds_read_b128 v[14:17], v14 offset:3072
	v_add_u32_e32 v191, 0x1c000, v176
	ds_read_b128 v[224:227], v191
	ds_read_b128 v[228:231], v191 offset:1024
	ds_read_b128 v[232:235], v191 offset:2048
	ds_read_b128 v[236:239], v191 offset:3072
	ds_read_b128 v[192:195], v177 offset:32768
	ds_read_b128 v[196:199], v177 offset:33792
	ds_read_b128 v[200:203], v177 offset:34816
	ds_read_b128 v[204:207], v177 offset:35840
	ds_read_b128 v[208:211], v177 offset:36864
	ds_read_b128 v[212:215], v177 offset:37888
	ds_read_b128 v[216:219], v177 offset:38912
	ds_read_b128 v[220:223], v177 offset:39936
	s_mov_b32 m0, s42
	s_nop 0
	buffer_load_dwordx4 v190, s[60:63], s8 offen lds
	s_mov_b32 m0, s43
	s_nop 0
	buffer_load_dwordx4 v189, s[60:63], s8 offen lds
	s_waitcnt vmcnt(8)
	s_waitcnt lgkmcnt(0)
	s_barrier
	s_setprio 1
	v_mfma_f32_16x16x128_f8f6f4 v[158:161], v[2:9], v[192:199], v[158:161]
	v_mfma_f32_16x16x128_f8f6f4 v[154:157], v[10:17], v[192:199], v[154:157]
	v_mfma_f32_16x16x128_f8f6f4 v[142:145], v[2:9], v[200:207], v[142:145]
	v_mfma_f32_16x16x128_f8f6f4 v[138:141], v[10:17], v[200:207], v[138:141]
	v_mfma_f32_16x16x128_f8f6f4 v[126:129], v[2:9], v[208:215], v[126:129]
	v_mfma_f32_16x16x128_f8f6f4 v[122:125], v[10:17], v[208:215], v[122:125]
	v_mfma_f32_16x16x128_f8f6f4 v[110:113], v[2:9], v[216:223], v[110:113]
	v_mfma_f32_16x16x128_f8f6f4 v[106:109], v[10:17], v[216:223], v[106:109]
	v_mfma_f32_16x16x128_f8f6f4 v[150:153], v[224:231], v[192:199], v[150:153]
	v_mfma_f32_16x16x128_f8f6f4 v[146:149], v[232:239], v[192:199], v[146:149]
	v_mfma_f32_16x16x128_f8f6f4 v[134:137], v[224:231], v[200:207], v[134:137]
	v_mfma_f32_16x16x128_f8f6f4 v[130:133], v[232:239], v[200:207], v[130:133]
	v_mfma_f32_16x16x128_f8f6f4 v[118:121], v[224:231], v[208:215], v[118:121]
	v_mfma_f32_16x16x128_f8f6f4 v[114:117], v[232:239], v[208:215], v[114:117]
	v_mfma_f32_16x16x128_f8f6f4 v[102:105], v[224:231], v[216:223], v[102:105]
	v_mfma_f32_16x16x128_f8f6f4 v[98:101], v[232:239], v[216:223], v[98:101]
	s_setprio 0
	s_barrier
	ds_read_b128 v[190:193], v177 offset:49152
	ds_read_b128 v[194:197], v177 offset:50176
	ds_read_b128 v[198:201], v177 offset:51200
	ds_read_b128 v[202:205], v177 offset:52224
	ds_read_b128 v[206:209], v177 offset:53248
	ds_read_b128 v[210:213], v177 offset:54272
	ds_read_b128 v[214:217], v177 offset:55296
	ds_read_b128 v[218:221], v177 offset:56320
	s_or_b32 s2, s2, 0x80
	s_mov_b32 m0, s44
	s_nop 0
	buffer_load_dwordx4 v173, s[64:67], s2 offen lds
	s_mov_b32 m0, s45
	s_nop 0
	buffer_load_dwordx4 v174, s[64:67], s2 offen lds
	s_add_i32 s3, s2, 0x40000
	s_mov_b32 m0, s48
	s_nop 0
	buffer_load_dwordx4 v173, s[64:67], s3 offen lds
	s_mov_b32 m0, s49
	s_nop 0
	buffer_load_dwordx4 v174, s[64:67], s3 offen lds
	s_mov_b32 m0, s46
	s_nop 0
	buffer_load_dwordx4 v187, s[60:63], s7 offen lds
	s_mov_b32 m0, s47
	s_nop 0
	buffer_load_dwordx4 v188, s[60:63], s7 offen lds
	s_waitcnt vmcnt(8)
	s_waitcnt lgkmcnt(0)
	s_barrier
	s_setprio 1
	v_mfma_f32_16x16x128_f8f6f4 v[94:97], v[2:9], v[190:197], v[94:97]
	v_mfma_f32_16x16x128_f8f6f4 v[90:93], v[10:17], v[190:197], v[90:93]
	v_mfma_f32_16x16x128_f8f6f4 v[78:81], v[2:9], v[198:205], v[78:81]
	v_mfma_f32_16x16x128_f8f6f4 v[74:77], v[10:17], v[198:205], v[74:77]
	v_mfma_f32_16x16x128_f8f6f4 v[62:65], v[2:9], v[206:213], v[62:65]
	v_mfma_f32_16x16x128_f8f6f4 v[58:61], v[10:17], v[206:213], v[58:61]
	v_mfma_f32_16x16x128_f8f6f4 v[46:49], v[2:9], v[214:221], v[46:49]
	v_mfma_f32_16x16x128_f8f6f4 v[42:45], v[10:17], v[214:221], v[42:45]
	v_mfma_f32_16x16x128_f8f6f4 v[86:89], v[224:231], v[190:197], v[86:89]
	v_mfma_f32_16x16x128_f8f6f4 v[82:85], v[232:239], v[190:197], v[82:85]
	v_mfma_f32_16x16x128_f8f6f4 v[70:73], v[224:231], v[198:205], v[70:73]
	v_mfma_f32_16x16x128_f8f6f4 v[66:69], v[232:239], v[198:205], v[66:69]
	v_mfma_f32_16x16x128_f8f6f4 v[54:57], v[224:231], v[206:213], v[54:57]
	v_mfma_f32_16x16x128_f8f6f4 v[50:53], v[232:239], v[206:213], v[50:53]
	v_mfma_f32_16x16x128_f8f6f4 v[38:41], v[224:231], v[214:221], v[38:41]
	v_mfma_f32_16x16x128_f8f6f4 v[34:37], v[232:239], v[214:221], v[34:37]
	s_setprio 0
	s_add_i32 s5, s5, 2
	s_addk_i32 s6, 0x100
	s_cmp_gt_u32 s5, 13
	s_barrier
	s_cbranch_scc1 .LBB0_934
;     __device__ __forceinline__ void operator()(const f32x4 (&acc)[2][2][4][2], const pg8::Unit& u, const Pre& pre, int wr, int wc, int fr, int fq) const {
;     ...
;         for (int i = 0; i < 8; ++i) { const int p = u.r0 + (i >> 2) * 128 + wr * 64 + (i & 3) * 16 + fr; rsv[i] = list_rs[e * LIST_STRIDE + (p < ce ? p : 0)]; }
.LBB0_932:
	s_cmp_eq_u32 s5, 12
	s_cselect_b64 s[2:3], -1, 0
	s_cmp_lg_u32 s5, 12
	v_mov_b32_e32 v189, v186
	v_mov_b32_e32 v190, v184
	v_mov_b32_e32 v187, v183
	v_mov_b32_e32 v188, v185
	s_cbranch_scc1 .LBB0_931
	global_load_dwordx4 v[22:25], v[168:169], off offset:16
	global_load_dwordx4 v[26:29], v[168:169], off
	global_load_dwordx4 v[18:21], v[166:167], off offset:16
	global_load_dwordx4 v[30:33], v[166:167], off
	v_mov_b32_e32 v189, v182
	v_mov_b32_e32 v190, v181
	v_mov_b32_e32 v187, v179
	v_mov_b32_e32 v188, v180
	s_lshl_b32 s8, s33, 2
	s_add_i32 s8, s8, 0x27e00
	v_mov_b32_e32 v247, s8
	ds_read_b32 v247, v247
	v_readfirstlane_b32 s8, v0
	s_lshl_b32 s98, s33, 14
	s_nop 2
	s_ashr_i32 s8, s8, 2
	s_andn2_b32 s8, s8, 63
	v_and_or_b32 v246, v0, 15, s8
	v_add_u32_e32 v246, s50, v246
	v_add_u32_e32 v241, 16, v246
	v_add_u32_e32 v242, 32, v246
	v_add_u32_e32 v243, 48, v246
	s_waitcnt lgkmcnt(0)
	v_cmp_lt_i32_e32 vcc, v246, v247
	v_cmp_lt_i32_e64 s[100:101], v241, v247
	s_nop 1
	v_cndmask_b32_e32 v240, 0, v246, vcc
	v_cndmask_b32_e64 v241, 0, v241, s[100:101]
	v_cmp_lt_i32_e32 vcc, v242, v247
	v_cmp_lt_i32_e64 s[100:101], v243, v247
	v_add_lshl_u32 v240, v240, s98, 2
	v_add_lshl_u32 v241, v241, s98, 2
	v_cndmask_b32_e32 v242, 0, v242, vcc
	v_cndmask_b32_e64 v243, 0, v243, s[100:101]
	global_load_dword v240, v240, s[28:29]
	global_load_dword v241, v241, s[28:29]
	v_add_lshl_u32 v242, v242, s98, 2
	v_add_lshl_u32 v243, v243, s98, 2
	v_add_u32_e32 v246, 0x80, v246
	global_load_dword v242, v242, s[28:29]
	global_load_dword v243, v243, s[28:29]
	v_sub_u32_e32 v247, v247, v246
	s_nop 0
	v_cmp_lt_i32_e32 vcc, 0, v247
	v_cmp_lt_i32_e64 s[100:101], 16, v247
	v_add_u32_e32 v247, 16, v246
	s_nop 0
	v_cndmask_b32_e32 v246, 0, v246, vcc
	v_cndmask_b32_e64 v247, 0, v247, s[100:101]
	v_add_lshl_u32 v246, v246, s98, 2
	v_add_lshl_u32 v247, v247, s98, 2
	global_load_dword v246, v246, s[28:29]
	global_load_dword v247, v247, s[28:29]
	s_branch .LBB0_931

; __device__ __forceinline__ unsigned cvt4_fp8(float a, float b, float c, float d) { int w = 0; w = __builtin_amdgcn_cvt_pk_fp8_f32(a, b, w, false); w = __builtin_amdgcn_cvt_pk_fp8_f32(c, d, w, true); return (unsigned)w; }
; __device__ __forceinline__ float sig1702_(float x) { return __builtin_amdgcn_rcpf(1.0f + __builtin_amdgcn_exp2f(x * -2.4554669f)); }
;     __device__ __forceinline__ void operator()(const f32x4 (&acc)[2][2][4][2], const pg8::Unit& u, const Pre& pre, int wr, int wc, int fr, int fq) const {
;     ...
;         for (int i = 0; i < 8; ++i) { const int p = u.r0 + (i >> 2) * 128 + wr * 64 + (i & 3) * 16 + fr; rsv[i] = list_rs[e * LIST_STRIDE + (p < ce ? p : 0)]; }
; #pragma unroll
;         for (int ai = 0; ai < 2; ++ai)
; #pragma unroll
;             for (int m = 0; m < 4; ++m) { const int rit = ai * 128 + wr * 64 + m * 16 + fr, p = u.r0 + rit; const float rs = (p < ce) ? rsv[ai * 4 + m] * 0.015625f : 0.f;
;                 f32x4 gt0 = acc[ai][0][m][0] * rs + g0, gt1 = acc[ai][0][m][1] * rs + g1, up0 = acc[ai][1][m][0] * rs + u0, up1 = acc[ai][1][m][1] * rs + u1;
;                 float o[8];
; #pragma unroll
;                 for (int j = 0; j < 4; ++j) { float gv = fminf(gt0[j], 7.0f), uv = fminf(fmaxf(up0[j], -7.0f), 7.0f); o[j] = (uv + 1.0f) * (gv * sig1702_(gv));
;                     gv = fminf(gt1[j], 7.0f); uv = fminf(fmaxf(up1[j], -7.0f), 7.0f); o[4 + j] = (uv + 1.0f) * (gv * sig1702_(gv)); }
;                 u32x2 w; w.x = cvt4_fp8(o[0], o[1], o[2], o[3]); w.y = cvt4_fp8(o[4], o[5], o[6], o[7]);
;                 *(u32x2*)(ACT + (size_t)(u.pm * 256 + rit) * DFF + col) = w; }
.LBB0_936:
	s_nop 15
	s_nop 3
	s_lshl_b32 s3, s33, 2
	s_add_i32 s3, s3, 0
	s_add_i32 s3, s3, 0x27e00
	v_mov_b32_e32 v6, v0
	v_mov_b32_e32 v2, s3
	ds_read_b32 v4, v2
	v_readfirstlane_b32 s2, v6
	s_ashr_i32 s3, s2, 2
	s_andn2_b32 s3, s3, 63
	v_and_or_b32 v5, v6, 15, s3
	v_add_u32_e32 v2, s50, v5
	s_waitcnt lgkmcnt(0)
	v_cmp_lt_i32_e64 s[8:9], v2, v4
	s_lshl_b32 s18, s33, 14
	v_add_u32_e32 v8, 0x80, v5
	v_cndmask_b32_e64 v2, 0, v2, s[8:9]
	v_add_u32_e32 v2, s18, v2
	v_ashrrev_i32_e32 v3, 31, v2
	v_lshl_add_u64 v[2:3], v[2:3], 2, s[28:29]
	v_mov_b32_e32 v183, v240
	v_add_u32_e32 v11, s50, v8
	s_lshl_b32 s3, s81, 7
	s_lshl_b32 s4, s33, 11
	s_lshr_b32 s2, s2, 1
	v_or_b32_e32 v186, 16, v5
	v_add_u32_e32 v12, 16, v11
	v_lshrrev_b32_e32 v2, 1, v6
	s_sub_i32 s3, s3, s4
	s_and_b32 s2, s2, 0x60
	v_or_b32_e32 v187, 32, v5
	v_or_b32_e32 v10, 48, v5
	v_add_u32_e32 v6, s50, v186
	v_add_u32_e32 v13, 32, v11
	v_cmp_lt_i32_e64 s[10:11], v12, v4
	s_or_b32 s2, s2, s3
	v_add_u32_e32 v7, s50, v187
	v_add_u32_e32 v9, s50, v10
	v_add_u32_e32 v14, 48, v11
	v_cmp_lt_i32_e64 s[6:7], v6, v4
	v_cndmask_b32_e64 v15, 0, v12, s[10:11]
	v_cmp_lt_i32_e64 s[10:11], v13, v4
	v_and_or_b32 v2, v2, 24, s2
	v_cndmask_b32_e64 v6, 0, v6, s[6:7]
	v_cmp_lt_i32_e64 s[4:5], v7, v4
	v_cmp_lt_i32_e64 s[2:3], v9, v4
	v_cmp_lt_i32_e32 vcc, v11, v4
	v_cndmask_b32_e64 v13, 0, v13, s[10:11]
	v_cmp_lt_i32_e64 s[10:11], v14, v4
	v_cndmask_b32_e64 v7, 0, v7, s[4:5]
	v_cndmask_b32_e64 v9, 0, v9, s[2:3]
	v_cndmask_b32_e32 v11, 0, v11, vcc
	v_cndmask_b32_e64 v17, 0, v14, s[10:11]
	v_add_u32_e32 v6, s18, v6
	v_add_u32_e32 v12, s18, v7
	v_add_u32_e32 v14, s18, v9
	v_add_u32_e32 v16, s18, v11
	v_add_u32_e32 v166, s18, v15
	v_add_u32_e32 v168, s18, v13
	v_add_u32_e32 v184, s18, v17
	v_ashrrev_i32_e32 v7, 31, v6
	v_ashrrev_i32_e32 v13, 31, v12
	v_ashrrev_i32_e32 v15, 31, v14
	v_ashrrev_i32_e32 v17, 31, v16
	v_ashrrev_i32_e32 v167, 31, v166
	v_ashrrev_i32_e32 v169, 31, v168
	v_ashrrev_i32_e32 v185, 31, v184
	v_lshl_add_u64 v[6:7], v[6:7], 2, s[28:29]
	v_lshl_add_u64 v[12:13], v[12:13], 2, s[28:29]
	v_lshl_add_u64 v[14:15], v[14:15], 2, s[28:29]
	v_lshl_add_u64 v[16:17], v[16:17], 2, s[28:29]
	v_lshl_add_u64 v[166:167], v[166:167], 2, s[28:29]
	v_lshl_add_u64 v[168:169], v[168:169], 2, s[28:29]
	v_lshl_add_u64 v[184:185], v[184:185], 2, s[28:29]
	v_mov_b32_e32 v188, v241
	v_mov_b32_e32 v189, v242
	v_mov_b32_e32 v190, v243
	v_mov_b32_e32 v11, v246
	v_mov_b32_e32 v9, v247
	s_nop 0
	global_load_dword v7, v[168:169], off
	global_load_dword v6, v[184:185], off
	v_ashrrev_i32_e32 v3, 31, v2
	s_waitcnt vmcnt(7)
	v_mul_f32_e32 v12, 0x3c800000, v183
	v_cndmask_b32_e64 v12, 0, v12, s[8:9]
	v_fma_f32 v13, v158, v12, v26
	v_min_f32_e32 v13, 0x40e00000, v13
	v_fma_f32 v16, v146, v12, v18
	v_mul_f32_e32 v146, 0xc01d265f, v13
	v_exp_f32_e32 v146, v146
	v_fma_f32 v14, v150, v12, v30
	v_fma_f32 v17, v159, v12, v27
	v_med3_f32 v14, v14, s73, v178
	v_add_f32_e32 v146, 1.0, v146
	v_rcp_f32_e32 v146, v146
	v_min_f32_e32 v17, 0x40e00000, v17
	v_fma_f32 v15, v154, v12, v22
	v_add_f32_e32 v14, 1.0, v14
	v_mul_f32_e32 v154, 0xc01d265f, v17
	v_mul_f32_e32 v13, v13, v146
	v_min_f32_e32 v15, 0x40e00000, v15
	v_mul_f32_e32 v13, v14, v13
	v_exp_f32_e32 v14, v154
	v_mul_f32_e32 v150, 0xc01d265f, v15
	v_exp_f32_e32 v150, v150
	v_med3_f32 v16, v16, s73, v178
	v_add_f32_e32 v14, 1.0, v14
	v_rcp_f32_e32 v14, v14
	v_add_f32_e32 v150, 1.0, v150
	v_rcp_f32_e32 v150, v150
	v_add_f32_e32 v16, 1.0, v16
	v_mul_f32_e32 v14, v17, v14
	v_fma_f32 v17, v155, v12, v23
	v_min_f32_e32 v17, 0x40e00000, v17
	v_mul_f32_e32 v15, v15, v150
	v_mul_f32_e32 v146, 0xc01d265f, v17
	v_mul_f32_e32 v15, v16, v15
	v_fma_f32 v16, v151, v12, v31
	v_exp_f32_e32 v146, v146
	v_med3_f32 v16, v16, s73, v178
	v_add_f32_e32 v16, 1.0, v16
	v_mul_f32_e32 v14, v16, v14
	v_fma_f32 v16, v147, v12, v19
	v_fma_f32 v147, v160, v12, v28
	v_add_f32_e32 v146, 1.0, v146
	v_min_f32_e32 v147, 0x40e00000, v147
	v_rcp_f32_e32 v146, v146
	v_mul_f32_e32 v150, 0xc01d265f, v147
	v_exp_f32_e32 v150, v150
	v_med3_f32 v16, v16, s73, v178
	v_add_f32_e32 v16, 1.0, v16
	v_mul_f32_e32 v17, v17, v146
	v_mul_f32_e32 v16, v16, v17
	v_add_f32_e32 v17, 1.0, v150
	v_rcp_f32_e32 v17, v17
	v_fma_f32 v146, v152, v12, v32
	v_med3_f32 v146, v146, s73, v178
	v_add_f32_e32 v146, 1.0, v146
	v_mul_f32_e32 v17, v147, v17
	v_fma_f32 v147, v156, v12, v24
	v_min_f32_e32 v147, 0x40e00000, v147
	v_mul_f32_e32 v150, 0xc01d265f, v147
	v_exp_f32_e32 v150, v150
	v_mul_f32_e32 v17, v146, v17
	v_fma_f32 v146, v148, v12, v20
	v_med3_f32 v146, v146, s73, v178
	v_add_f32_e32 v148, 1.0, v150
	v_fma_f32 v150, v161, v12, v29
	v_min_f32_e32 v150, 0x40e00000, v150
	v_rcp_f32_e32 v148, v148
	v_mul_f32_e32 v151, 0xc01d265f, v150
	v_exp_f32_e32 v151, v151
	v_add_f32_e32 v146, 1.0, v146
	v_mul_f32_e32 v147, v147, v148
	v_mul_f32_e32 v146, v146, v147
	v_add_f32_e32 v147, 1.0, v151
	v_rcp_f32_e32 v147, v147
	v_fma_f32 v148, v153, v12, v33
	v_med3_f32 v148, v148, s73, v178
	v_add_f32_e32 v148, 1.0, v148
	v_mul_f32_e32 v147, v150, v147
	v_mul_f32_e32 v147, v148, v147
	v_fma_f32 v148, v157, v12, v25
	v_min_f32_e32 v148, 0x40e00000, v148
	v_mul_f32_e32 v150, 0xc01d265f, v148
	v_exp_f32_e32 v150, v150
	v_fma_f32 v12, v149, v12, v21
	v_med3_f32 v12, v12, s73, v178
	v_add_f32_e32 v149, 1.0, v12
	v_add_f32_e32 v12, 1.0, v150
	v_rcp_f32_e32 v150, v12
	v_mov_b32_e32 v12, 0
	v_cvt_pk_fp8_f32 v12, v13, v14
	v_mov_b32_e32 v13, 0
	v_cvt_pk_fp8_f32 v13, v15, v16
	s_waitcnt vmcnt(6)
; __device__ __forceinline__ unsigned cvt4_fp8(float a, float b, float c, float d) { int w = 0; w = __builtin_amdgcn_cvt_pk_fp8_f32(a, b, w, false); w = __builtin_amdgcn_cvt_pk_fp8_f32(c, d, w, true); return (unsigned)w; }
; __device__ __forceinline__ float sig1702_(float x) { return __builtin_amdgcn_rcpf(1.0f + __builtin_amdgcn_exp2f(x * -2.4554669f)); }
;     __device__ __forceinline__ void operator()(const f32x4 (&acc)[2][2][4][2], const pg8::Unit& u, const Pre& pre, int wr, int wc, int fr, int fq) const {
;     ...
;             for (int m = 0; m < 4; ++m) { const int rit = ai * 128 + wr * 64 + m * 16 + fr, p = u.r0 + rit; const float rs = (p < ce) ? rsv[ai * 4 + m] * 0.015625f : 0.f;
;                 f32x4 gt0 = acc[ai][0][m][0] * rs + g0, gt1 = acc[ai][0][m][1] * rs + g1, up0 = acc[ai][1][m][0] * rs + u0, up1 = acc[ai][1][m][1] * rs + u1;
;                 float o[8];
; #pragma unroll
;                 for (int j = 0; j < 4; ++j) { float gv = fminf(gt0[j], 7.0f), uv = fminf(fmaxf(up0[j], -7.0f), 7.0f); o[j] = (uv + 1.0f) * (gv * sig1702_(gv));
;                     gv = fminf(gt1[j], 7.0f); uv = fminf(fmaxf(up1[j], -7.0f), 7.0f); o[4 + j] = (uv + 1.0f) * (gv * sig1702_(gv)); }
;                 u32x2 w; w.x = cvt4_fp8(o[0], o[1], o[2], o[3]); w.y = cvt4_fp8(o[4], o[5], o[6], o[7]);
;                 *(u32x2*)(ACT + (size_t)(u.pm * 256 + rit) * DFF + col) = w; }
	v_mul_f32_e32 v16, 0x3c800000, v188
	v_mul_f32_e32 v14, v148, v150
	v_cndmask_b32_e64 v16, 0, v16, s[6:7]
	v_mul_f32_e32 v14, v149, v14
	v_cvt_pk_fp8_f32 v12, v17, v147 op_sel:[0,0,1]
	s_lshl_b32 s8, s79, 8
	v_fma_f32 v17, v142, v16, v26
	v_cvt_pk_fp8_f32 v13, v146, v14 op_sel:[0,0,1]
	v_add_u32_e32 v14, s8, v5
	v_min_f32_e32 v17, 0x40e00000, v17
	v_ashrrev_i32_e32 v15, 31, v14
	v_mul_f32_e32 v142, 0xc01d265f, v17
	v_lshlrev_b64 v[14:15], 11, v[14:15]
	v_exp_f32_e32 v142, v142
	v_lshl_add_u64 v[14:15], s[26:27], 0, v[14:15]
	v_lshl_add_u64 v[14:15], v[14:15], 0, v[2:3]
	global_store_dwordx2 v[14:15], v[12:13], off
	v_fma_f32 v14, v138, v16, v22
	v_add_f32_e32 v12, 1.0, v142
	v_min_f32_e32 v14, 0x40e00000, v14
	v_rcp_f32_e32 v12, v12
	v_mul_f32_e32 v15, 0xc01d265f, v14
	v_exp_f32_e32 v15, v15
	v_fma_f32 v13, v134, v16, v30
	v_med3_f32 v13, v13, s73, v178
	v_mul_f32_e32 v12, v17, v12
	v_fma_f32 v17, v143, v16, v27
	v_add_f32_e32 v13, 1.0, v13
	v_add_f32_e32 v15, 1.0, v15
	v_min_f32_e32 v17, 0x40e00000, v17
	v_mul_f32_e32 v13, v13, v12
	v_fma_f32 v12, v130, v16, v18
	v_rcp_f32_e32 v15, v15
	v_mul_f32_e32 v130, 0xc01d265f, v17
	v_exp_f32_e32 v130, v130
	v_med3_f32 v12, v12, s73, v178
	v_add_f32_e32 v12, 1.0, v12
	v_mul_f32_e32 v14, v14, v15
	v_mul_f32_e32 v14, v12, v14
	v_add_f32_e32 v12, 1.0, v130
	v_rcp_f32_e32 v12, v12
	v_fma_f32 v15, v135, v16, v31
	v_med3_f32 v15, v15, s73, v178
	v_add_f32_e32 v15, 1.0, v15
	v_mul_f32_e32 v12, v17, v12
	v_fma_f32 v17, v139, v16, v23
	v_min_f32_e32 v17, 0x40e00000, v17
	v_mul_f32_e32 v130, 0xc01d265f, v17
	v_exp_f32_e32 v130, v130
	v_mul_f32_e32 v15, v15, v12
	v_fma_f32 v12, v131, v16, v19
	v_fma_f32 v131, v144, v16, v28
	v_add_f32_e32 v130, 1.0, v130
	v_min_f32_e32 v131, 0x40e00000, v131
	v_rcp_f32_e32 v130, v130
	v_mul_f32_e32 v134, 0xc01d265f, v131
	v_exp_f32_e32 v134, v134
	v_med3_f32 v12, v12, s73, v178
	v_add_f32_e32 v12, 1.0, v12
	v_mul_f32_e32 v17, v17, v130
	v_mul_f32_e32 v17, v12, v17
	v_add_f32_e32 v12, 1.0, v134
	v_rcp_f32_e32 v12, v12
	v_fma_f32 v130, v136, v16, v32
	v_med3_f32 v130, v130, s73, v178
	v_add_f32_e32 v130, 1.0, v130
	v_mul_f32_e32 v12, v131, v12
	v_fma_f32 v131, v140, v16, v24
	v_min_f32_e32 v131, 0x40e00000, v131
	v_mul_f32_e32 v134, 0xc01d265f, v131
	v_exp_f32_e32 v134, v134
	v_mul_f32_e32 v130, v130, v12
	v_fma_f32 v12, v132, v16, v20
	v_med3_f32 v12, v12, s73, v178
	v_add_f32_e32 v132, 1.0, v134
	v_fma_f32 v134, v145, v16, v29
	v_min_f32_e32 v134, 0x40e00000, v134
	v_rcp_f32_e32 v132, v132
	v_mul_f32_e32 v135, 0xc01d265f, v134
	v_exp_f32_e32 v135, v135
	v_add_f32_e32 v12, 1.0, v12
	v_mul_f32_e32 v131, v131, v132
	v_mul_f32_e32 v131, v12, v131
	v_add_f32_e32 v12, 1.0, v135
	v_rcp_f32_e32 v12, v12
	v_fma_f32 v132, v137, v16, v33
	v_med3_f32 v132, v132, s73, v178
	v_add_f32_e32 v132, 1.0, v132
	v_mul_f32_e32 v12, v134, v12
	v_mul_f32_e32 v132, v132, v12
	v_fma_f32 v12, v141, v16, v25
	v_min_f32_e32 v134, 0x40e00000, v12
	v_mul_f32_e32 v12, 0xc01d265f, v134
	v_exp_f32_e32 v12, v12
	v_fma_f32 v16, v133, v16, v21
	v_med3_f32 v16, v16, s73, v178
	v_add_f32_e32 v16, 1.0, v16
	v_add_f32_e32 v12, 1.0, v12
	v_rcp_f32_e32 v133, v12
	v_mov_b32_e32 v12, 0
	v_cvt_pk_fp8_f32 v12, v13, v15
	v_mov_b32_e32 v13, 0
	v_cvt_pk_fp8_f32 v13, v14, v17
	v_mul_f32_e32 v14, v134, v133
	v_mul_f32_e32 v14, v16, v14
	s_waitcnt vmcnt(6)
	v_mul_f32_e32 v16, 0x3c800000, v189
	v_cndmask_b32_e64 v16, 0, v16, s[4:5]
	v_fma_f32 v17, v126, v16, v26
	v_cvt_pk_fp8_f32 v13, v131, v14 op_sel:[0,0,1]
	v_add_u32_e32 v14, s8, v186
	v_min_f32_e32 v17, 0x40e00000, v17
	v_cvt_pk_fp8_f32 v12, v130, v132 op_sel:[0,0,1]
	v_ashrrev_i32_e32 v15, 31, v14
	v_mul_f32_e32 v126, 0xc01d265f, v17
	v_lshlrev_b64 v[14:15], 11, v[14:15]
	v_exp_f32_e32 v126, v126
	v_lshl_add_u64 v[14:15], s[26:27], 0, v[14:15]
	v_lshl_add_u64 v[14:15], v[14:15], 0, v[2:3]
	global_store_dwordx2 v[14:15], v[12:13], off
	v_fma_f32 v14, v122, v16, v22
	v_add_f32_e32 v12, 1.0, v126
	v_min_f32_e32 v14, 0x40e00000, v14
	v_rcp_f32_e32 v12, v12
	v_mul_f32_e32 v15, 0xc01d265f, v14
	v_exp_f32_e32 v15, v15
	v_fma_f32 v13, v118, v16, v30
	v_med3_f32 v13, v13, s73, v178
	v_mul_f32_e32 v12, v17, v12
	v_fma_f32 v17, v127, v16, v27
	v_add_f32_e32 v13, 1.0, v13
	v_add_f32_e32 v15, 1.0, v15
	v_min_f32_e32 v17, 0x40e00000, v17
	v_mul_f32_e32 v13, v13, v12
	v_fma_f32 v12, v114, v16, v18
	v_rcp_f32_e32 v15, v15
	v_mul_f32_e32 v114, 0xc01d265f, v17
	v_exp_f32_e32 v114, v114
	v_med3_f32 v12, v12, s73, v178
	v_add_f32_e32 v12, 1.0, v12
	v_mul_f32_e32 v14, v14, v15
	v_mul_f32_e32 v14, v12, v14
	v_add_f32_e32 v12, 1.0, v114
	v_rcp_f32_e32 v12, v12
	v_fma_f32 v15, v119, v16, v31
	v_med3_f32 v15, v15, s73, v178
	v_add_f32_e32 v15, 1.0, v15
	v_mul_f32_e32 v12, v17, v12
	v_fma_f32 v17, v123, v16, v23
	v_min_f32_e32 v17, 0x40e00000, v17
	v_mul_f32_e32 v114, 0xc01d265f, v17
	v_exp_f32_e32 v114, v114
	v_mul_f32_e32 v15, v15, v12
	v_fma_f32 v12, v115, v16, v19
	v_fma_f32 v115, v128, v16, v28
	v_add_f32_e32 v114, 1.0, v114
	v_min_f32_e32 v115, 0x40e00000, v115
	v_rcp_f32_e32 v114, v114
	v_mul_f32_e32 v118, 0xc01d265f, v115
	v_exp_f32_e32 v118, v118
	v_med3_f32 v12, v12, s73, v178
	v_add_f32_e32 v12, 1.0, v12
	v_mul_f32_e32 v17, v17, v114
	v_mul_f32_e32 v17, v12, v17
	v_add_f32_e32 v12, 1.0, v118
	v_rcp_f32_e32 v12, v12
	v_fma_f32 v114, v120, v16, v32
	v_med3_f32 v114, v114, s73, v178
	v_add_f32_e32 v114, 1.0, v114
	v_mul_f32_e32 v12, v115, v12
	v_fma_f32 v115, v124, v16, v24
	v_min_f32_e32 v115, 0x40e00000, v115
	v_mul_f32_e32 v118, 0xc01d265f, v115
	v_exp_f32_e32 v118, v118
	v_mul_f32_e32 v114, v114, v12
	v_fma_f32 v12, v116, v16, v20
	v_med3_f32 v12, v12, s73, v178
	v_add_f32_e32 v116, 1.0, v118
	v_fma_f32 v118, v129, v16, v29
	v_min_f32_e32 v118, 0x40e00000, v118
	v_rcp_f32_e32 v116, v116
	v_mul_f32_e32 v119, 0xc01d265f, v118
	v_exp_f32_e32 v119, v119
	v_add_f32_e32 v12, 1.0, v12
	v_mul_f32_e32 v115, v115, v116
	v_mul_f32_e32 v115, v12, v115
	v_add_f32_e32 v12, 1.0, v119
	v_rcp_f32_e32 v12, v12
	v_fma_f32 v116, v121, v16, v33
	v_med3_f32 v116, v116, s73, v178
	v_add_f32_e32 v116, 1.0, v116
	v_mul_f32_e32 v12, v118, v12
	v_mul_f32_e32 v116, v116, v12
	v_fma_f32 v12, v125, v16, v25
	v_min_f32_e32 v118, 0x40e00000, v12
	v_mul_f32_e32 v12, 0xc01d265f, v118
	v_exp_f32_e32 v12, v12
	v_fma_f32 v16, v117, v16, v21
	v_med3_f32 v16, v16, s73, v178
	v_add_f32_e32 v16, 1.0, v16
	v_add_f32_e32 v12, 1.0, v12
	v_rcp_f32_e32 v117, v12
	v_mov_b32_e32 v12, 0
	v_cvt_pk_fp8_f32 v12, v13, v15
	v_mov_b32_e32 v13, 0
	v_cvt_pk_fp8_f32 v13, v14, v17
	v_mul_f32_e32 v14, v118, v117
	v_mul_f32_e32 v14, v16, v14
	s_waitcnt vmcnt(6)
; __device__ __forceinline__ unsigned cvt4_fp8(float a, float b, float c, float d) { int w = 0; w = __builtin_amdgcn_cvt_pk_fp8_f32(a, b, w, false); w = __builtin_amdgcn_cvt_pk_fp8_f32(c, d, w, true); return (unsigned)w; }
; __device__ __forceinline__ float sig1702_(float x) { return __builtin_amdgcn_rcpf(1.0f + __builtin_amdgcn_exp2f(x * -2.4554669f)); }
;     __device__ __forceinline__ void operator()(const f32x4 (&acc)[2][2][4][2], const pg8::Unit& u, const Pre& pre, int wr, int wc, int fr, int fq) const {
;     ...
;         for (int i = 0; i < 8; ++i) { const int p = u.r0 + (i >> 2) * 128 + wr * 64 + (i & 3) * 16 + fr; rsv[i] = list_rs[e * LIST_STRIDE + (p < ce ? p : 0)]; }
; #pragma unroll
;         for (int ai = 0; ai < 2; ++ai)
; #pragma unroll
;             for (int m = 0; m < 4; ++m) { const int rit = ai * 128 + wr * 64 + m * 16 + fr, p = u.r0 + rit; const float rs = (p < ce) ? rsv[ai * 4 + m] * 0.015625f : 0.f;
;                 f32x4 gt0 = acc[ai][0][m][0] * rs + g0, gt1 = acc[ai][0][m][1] * rs + g1, up0 = acc[ai][1][m][0] * rs + u0, up1 = acc[ai][1][m][1] * rs + u1;
;                 float o[8];
; #pragma unroll
;                 for (int j = 0; j < 4; ++j) { float gv = fminf(gt0[j], 7.0f), uv = fminf(fmaxf(up0[j], -7.0f), 7.0f); o[j] = (uv + 1.0f) * (gv * sig1702_(gv));
;                     gv = fminf(gt1[j], 7.0f); uv = fminf(fmaxf(up1[j], -7.0f), 7.0f); o[4 + j] = (uv + 1.0f) * (gv * sig1702_(gv)); }
;                 u32x2 w; w.x = cvt4_fp8(o[0], o[1], o[2], o[3]); w.y = cvt4_fp8(o[4], o[5], o[6], o[7]);
;                 *(u32x2*)(ACT + (size_t)(u.pm * 256 + rit) * DFF + col) = w; }
	v_mul_f32_e32 v16, 0x3c800000, v190
	v_cndmask_b32_e64 v16, 0, v16, s[2:3]
	v_fma_f32 v17, v110, v16, v26
	v_cvt_pk_fp8_f32 v13, v115, v14 op_sel:[0,0,1]
	v_add_u32_e32 v14, s8, v187
	v_min_f32_e32 v17, 0x40e00000, v17
	v_cvt_pk_fp8_f32 v12, v114, v116 op_sel:[0,0,1]
	v_ashrrev_i32_e32 v15, 31, v14
	v_mul_f32_e32 v110, 0xc01d265f, v17
	v_lshlrev_b64 v[14:15], 11, v[14:15]
	v_exp_f32_e32 v110, v110
	v_lshl_add_u64 v[14:15], s[26:27], 0, v[14:15]
	v_lshl_add_u64 v[14:15], v[14:15], 0, v[2:3]
	global_store_dwordx2 v[14:15], v[12:13], off
	v_fma_f32 v14, v106, v16, v22
	v_add_f32_e32 v12, 1.0, v110
	v_min_f32_e32 v14, 0x40e00000, v14
	v_rcp_f32_e32 v12, v12
	v_mul_f32_e32 v15, 0xc01d265f, v14
	v_exp_f32_e32 v15, v15
	v_fma_f32 v13, v102, v16, v30
	v_med3_f32 v13, v13, s73, v178
	v_mul_f32_e32 v12, v17, v12
	v_fma_f32 v17, v111, v16, v27
	v_add_f32_e32 v13, 1.0, v13
	v_add_f32_e32 v15, 1.0, v15
	v_min_f32_e32 v17, 0x40e00000, v17
	v_mul_f32_e32 v13, v13, v12
	v_fma_f32 v12, v98, v16, v18
	v_rcp_f32_e32 v15, v15
	v_mul_f32_e32 v98, 0xc01d265f, v17
	v_exp_f32_e32 v98, v98
	v_med3_f32 v12, v12, s73, v178
	v_add_f32_e32 v12, 1.0, v12
	v_mul_f32_e32 v14, v14, v15
	v_mul_f32_e32 v14, v12, v14
	v_add_f32_e32 v12, 1.0, v98
	v_rcp_f32_e32 v12, v12
	v_fma_f32 v15, v103, v16, v31
	v_med3_f32 v15, v15, s73, v178
	v_add_f32_e32 v15, 1.0, v15
	v_mul_f32_e32 v12, v17, v12
	v_fma_f32 v17, v107, v16, v23
	v_min_f32_e32 v17, 0x40e00000, v17
	v_mul_f32_e32 v98, 0xc01d265f, v17
	v_exp_f32_e32 v98, v98
	v_mul_f32_e32 v15, v15, v12
	v_fma_f32 v12, v99, v16, v19
	v_fma_f32 v99, v112, v16, v28
	v_add_f32_e32 v98, 1.0, v98
	v_min_f32_e32 v99, 0x40e00000, v99
	v_rcp_f32_e32 v98, v98
	v_mul_f32_e32 v102, 0xc01d265f, v99
	v_exp_f32_e32 v102, v102
	v_med3_f32 v12, v12, s73, v178
	v_add_f32_e32 v12, 1.0, v12
	v_mul_f32_e32 v17, v17, v98
	v_mul_f32_e32 v17, v12, v17
	v_add_f32_e32 v12, 1.0, v102
	v_rcp_f32_e32 v12, v12
	v_fma_f32 v98, v104, v16, v32
	v_med3_f32 v98, v98, s73, v178
	v_add_f32_e32 v98, 1.0, v98
	v_mul_f32_e32 v12, v99, v12
	v_fma_f32 v99, v108, v16, v24
	v_min_f32_e32 v99, 0x40e00000, v99
	v_mul_f32_e32 v102, 0xc01d265f, v99
	v_exp_f32_e32 v102, v102
	v_mul_f32_e32 v98, v98, v12
	v_fma_f32 v12, v100, v16, v20
	v_med3_f32 v12, v12, s73, v178
	v_add_f32_e32 v100, 1.0, v102
	v_fma_f32 v102, v113, v16, v29
	v_min_f32_e32 v102, 0x40e00000, v102
	v_rcp_f32_e32 v100, v100
	v_mul_f32_e32 v103, 0xc01d265f, v102
	v_exp_f32_e32 v103, v103
	v_add_f32_e32 v12, 1.0, v12
	v_mul_f32_e32 v99, v99, v100
	v_mul_f32_e32 v99, v12, v99
	v_add_f32_e32 v12, 1.0, v103
	v_rcp_f32_e32 v12, v12
	v_fma_f32 v100, v105, v16, v33
	v_med3_f32 v100, v100, s73, v178
	v_add_f32_e32 v100, 1.0, v100
	v_mul_f32_e32 v12, v102, v12
	v_mul_f32_e32 v100, v100, v12
	v_fma_f32 v12, v109, v16, v25
	v_min_f32_e32 v102, 0x40e00000, v12
	v_mul_f32_e32 v12, 0xc01d265f, v102
	v_exp_f32_e32 v12, v12
	v_fma_f32 v16, v101, v16, v21
	v_med3_f32 v16, v16, s73, v178
	v_add_f32_e32 v16, 1.0, v16
	v_add_f32_e32 v12, 1.0, v12
	v_rcp_f32_e32 v101, v12
	v_mov_b32_e32 v12, 0
	v_cvt_pk_fp8_f32 v12, v13, v15
	v_mov_b32_e32 v13, 0
	v_cvt_pk_fp8_f32 v13, v14, v17
	v_mul_f32_e32 v14, v102, v101
	v_mul_f32_e32 v14, v16, v14
	v_cvt_pk_fp8_f32 v12, v98, v100 op_sel:[0,0,1]
	v_cvt_pk_fp8_f32 v13, v99, v14 op_sel:[0,0,1]
	v_add_u32_e32 v14, s8, v10
	s_waitcnt vmcnt(6)
	v_mul_f32_e32 v10, 0x3c800000, v11
	v_cndmask_b32_e32 v16, 0, v10, vcc
	v_fma_f32 v10, v94, v16, v26
	v_ashrrev_i32_e32 v15, 31, v14
	v_min_f32_e32 v17, 0x40e00000, v10
	v_lshlrev_b64 v[14:15], 11, v[14:15]
	v_mul_f32_e32 v10, 0xc01d265f, v17
	v_exp_f32_e32 v94, v10
	v_lshl_add_u64 v[10:11], s[26:27], 0, v[14:15]
	v_lshl_add_u64 v[10:11], v[10:11], 0, v[2:3]
	global_store_dwordx2 v[10:11], v[12:13], off
	v_fma_f32 v12, v90, v16, v22
	v_min_f32_e32 v12, 0x40e00000, v12
	v_mul_f32_e32 v13, 0xc01d265f, v12
	v_exp_f32_e32 v13, v13
	v_add_f32_e32 v10, 1.0, v94
	v_rcp_f32_e32 v10, v10
	v_fma_f32 v14, v95, v16, v27
	v_fma_f32 v11, v86, v16, v30
	v_add_f32_e32 v13, 1.0, v13
	v_min_f32_e32 v14, 0x40e00000, v14
	v_med3_f32 v11, v11, s73, v178
	v_rcp_f32_e32 v13, v13
	v_mul_f32_e32 v15, 0xc01d265f, v14
	v_add_f32_e32 v11, 1.0, v11
	v_mul_f32_e32 v10, v17, v10
	v_exp_f32_e32 v15, v15
	v_mul_f32_e32 v11, v11, v10
	v_fma_f32 v10, v82, v16, v18
	v_med3_f32 v10, v10, s73, v178
	v_add_f32_e32 v10, 1.0, v10
	v_mul_f32_e32 v12, v12, v13
	v_mul_f32_e32 v12, v10, v12
	v_add_f32_e32 v10, 1.0, v15
	v_rcp_f32_e32 v10, v10
	v_fma_f32 v17, v96, v16, v28
	v_fma_f32 v13, v87, v16, v31
	v_min_f32_e32 v17, 0x40e00000, v17
	v_mul_f32_e32 v10, v14, v10
	v_fma_f32 v14, v91, v16, v23
	v_min_f32_e32 v14, 0x40e00000, v14
	v_mul_f32_e32 v15, 0xc01d265f, v14
	v_exp_f32_e32 v15, v15
	v_med3_f32 v13, v13, s73, v178
	v_mul_f32_e32 v82, 0xc01d265f, v17
	v_add_f32_e32 v13, 1.0, v13
	v_add_f32_e32 v15, 1.0, v15
	v_rcp_f32_e32 v15, v15
	v_exp_f32_e32 v82, v82
	v_mul_f32_e32 v13, v13, v10
	v_fma_f32 v10, v83, v16, v19
	v_med3_f32 v10, v10, s73, v178
	v_add_f32_e32 v10, 1.0, v10
	v_mul_f32_e32 v14, v14, v15
	v_mul_f32_e32 v14, v10, v14
	v_add_f32_e32 v10, 1.0, v82
	v_rcp_f32_e32 v10, v10
	v_fma_f32 v15, v88, v16, v32
	v_med3_f32 v15, v15, s73, v178
	v_fma_f32 v83, v97, v16, v29
	v_mul_f32_e32 v10, v17, v10
	v_fma_f32 v17, v92, v16, v24
	v_min_f32_e32 v17, 0x40e00000, v17
	v_mul_f32_e32 v82, 0xc01d265f, v17
	v_exp_f32_e32 v82, v82
	v_add_f32_e32 v15, 1.0, v15
	v_min_f32_e32 v83, 0x40e00000, v83
	v_mul_f32_e32 v15, v15, v10
	v_add_f32_e32 v82, 1.0, v82
	v_fma_f32 v10, v84, v16, v20
	v_rcp_f32_e32 v82, v82
	v_mul_f32_e32 v84, 0xc01d265f, v83
	v_exp_f32_e32 v84, v84
	v_med3_f32 v10, v10, s73, v178
	v_add_f32_e32 v10, 1.0, v10
	v_mul_f32_e32 v17, v17, v82
	v_mul_f32_e32 v17, v10, v17
	v_add_f32_e32 v10, 1.0, v84
	v_rcp_f32_e32 v10, v10
	v_fma_f32 v82, v89, v16, v33
	v_med3_f32 v82, v82, s73, v178
	v_add_f32_e32 v82, 1.0, v82
	v_mul_f32_e32 v10, v83, v10
	v_mul_f32_e32 v82, v82, v10
	v_fma_f32 v10, v93, v16, v25
	v_min_f32_e32 v83, 0x40e00000, v10
	v_mul_f32_e32 v10, 0xc01d265f, v83
	v_exp_f32_e32 v10, v10
	v_fma_f32 v16, v85, v16, v21
	v_med3_f32 v16, v16, s73, v178
	v_add_f32_e32 v16, 1.0, v16
	v_add_f32_e32 v10, 1.0, v10
	v_rcp_f32_e32 v84, v10
	v_mov_b32_e32 v10, 0
	v_cvt_pk_fp8_f32 v10, v11, v13
	v_mov_b32_e32 v11, 0
	v_cvt_pk_fp8_f32 v11, v12, v14
	v_mul_f32_e32 v12, v83, v84
	v_mul_f32_e32 v12, v16, v12
	v_add_u32_e32 v14, 0x90, v5
	v_cvt_pk_fp8_f32 v11, v17, v12 op_sel:[0,0,1]
	v_add_u32_e32 v12, s8, v8
	v_add_u32_e32 v8, s50, v14
	s_waitcnt vmcnt(6)
; __device__ __forceinline__ unsigned cvt4_fp8(float a, float b, float c, float d) { int w = 0; w = __builtin_amdgcn_cvt_pk_fp8_f32(a, b, w, false); w = __builtin_amdgcn_cvt_pk_fp8_f32(c, d, w, true); return (unsigned)w; }
; __device__ __forceinline__ float sig1702_(float x) { return __builtin_amdgcn_rcpf(1.0f + __builtin_amdgcn_exp2f(x * -2.4554669f)); }
;     __device__ __forceinline__ void operator()(const f32x4 (&acc)[2][2][4][2], const pg8::Unit& u, const Pre& pre, int wr, int wc, int fr, int fq) const {
;     ...
;             for (int m = 0; m < 4; ++m) { const int rit = ai * 128 + wr * 64 + m * 16 + fr, p = u.r0 + rit; const float rs = (p < ce) ? rsv[ai * 4 + m] * 0.015625f : 0.f;
;                 f32x4 gt0 = acc[ai][0][m][0] * rs + g0, gt1 = acc[ai][0][m][1] * rs + g1, up0 = acc[ai][1][m][0] * rs + u0, up1 = acc[ai][1][m][1] * rs + u1;
;                 float o[8];
; #pragma unroll
;                 for (int j = 0; j < 4; ++j) { float gv = fminf(gt0[j], 7.0f), uv = fminf(fmaxf(up0[j], -7.0f), 7.0f); o[j] = (uv + 1.0f) * (gv * sig1702_(gv));
;                     gv = fminf(gt1[j], 7.0f); uv = fminf(fmaxf(up1[j], -7.0f), 7.0f); o[4 + j] = (uv + 1.0f) * (gv * sig1702_(gv)); }
;                 u32x2 w; w.x = cvt4_fp8(o[0], o[1], o[2], o[3]); w.y = cvt4_fp8(o[4], o[5], o[6], o[7]);
;                 *(u32x2*)(ACT + (size_t)(u.pm * 256 + rit) * DFF + col) = w; }
	v_mul_f32_e32 v9, 0x3c800000, v9
	v_cmp_lt_i32_e32 vcc, v8, v4
	v_cvt_pk_fp8_f32 v10, v15, v82 op_sel:[0,0,1]
	v_ashrrev_i32_e32 v13, 31, v12
	v_cndmask_b32_e32 v15, 0, v9, vcc
	v_fma_f32 v8, v78, v15, v26
	v_min_f32_e32 v16, 0x40e00000, v8
	v_lshlrev_b64 v[12:13], 11, v[12:13]
	v_mul_f32_e32 v8, 0xc01d265f, v16
	v_exp_f32_e32 v17, v8
	v_lshl_add_u64 v[8:9], s[26:27], 0, v[12:13]
	v_lshl_add_u64 v[8:9], v[8:9], 0, v[2:3]
	global_store_dwordx2 v[8:9], v[10:11], off
	v_fma_f32 v10, v74, v15, v22
	v_min_f32_e32 v10, 0x40e00000, v10
	v_mul_f32_e32 v11, 0xc01d265f, v10
	v_exp_f32_e32 v11, v11
	v_add_f32_e32 v8, 1.0, v17
	v_rcp_f32_e32 v8, v8
	v_fma_f32 v12, v79, v15, v27
	v_fma_f32 v9, v70, v15, v30
	v_add_f32_e32 v11, 1.0, v11
	v_min_f32_e32 v12, 0x40e00000, v12
	v_med3_f32 v9, v9, s73, v178
	v_rcp_f32_e32 v11, v11
	v_mul_f32_e32 v13, 0xc01d265f, v12
	v_add_f32_e32 v9, 1.0, v9
	v_mul_f32_e32 v8, v16, v8
	v_exp_f32_e32 v13, v13
	v_mul_f32_e32 v9, v9, v8
	v_fma_f32 v8, v66, v15, v18
	v_med3_f32 v8, v8, s73, v178
	v_add_f32_e32 v8, 1.0, v8
	v_mul_f32_e32 v10, v10, v11
	v_mul_f32_e32 v10, v8, v10
	v_add_f32_e32 v8, 1.0, v13
	v_rcp_f32_e32 v8, v8
	v_fma_f32 v16, v80, v15, v28
	v_fma_f32 v11, v71, v15, v31
	v_min_f32_e32 v16, 0x40e00000, v16
	v_mul_f32_e32 v8, v12, v8
	v_fma_f32 v12, v75, v15, v23
	v_min_f32_e32 v12, 0x40e00000, v12
	v_mul_f32_e32 v13, 0xc01d265f, v12
	v_exp_f32_e32 v13, v13
	v_med3_f32 v11, v11, s73, v178
	v_mul_f32_e32 v17, 0xc01d265f, v16
	v_add_f32_e32 v11, 1.0, v11
	v_add_f32_e32 v13, 1.0, v13
	v_rcp_f32_e32 v13, v13
	v_exp_f32_e32 v17, v17
	v_mul_f32_e32 v11, v11, v8
	v_fma_f32 v8, v67, v15, v19
	v_med3_f32 v8, v8, s73, v178
	v_add_f32_e32 v8, 1.0, v8
	v_mul_f32_e32 v12, v12, v13
	v_mul_f32_e32 v12, v8, v12
	v_add_f32_e32 v8, 1.0, v17
	v_rcp_f32_e32 v8, v8
	v_fma_f32 v66, v81, v15, v29
	v_fma_f32 v13, v72, v15, v32
	v_min_f32_e32 v66, 0x40e00000, v66
	v_mul_f32_e32 v8, v16, v8
	v_fma_f32 v16, v76, v15, v24
	v_min_f32_e32 v16, 0x40e00000, v16
	v_mul_f32_e32 v17, 0xc01d265f, v16
	v_exp_f32_e32 v17, v17
	v_med3_f32 v13, v13, s73, v178
	v_mul_f32_e32 v67, 0xc01d265f, v66
	v_add_f32_e32 v13, 1.0, v13
	v_add_f32_e32 v17, 1.0, v17
	v_rcp_f32_e32 v17, v17
	v_exp_f32_e32 v67, v67
	v_mul_f32_e32 v13, v13, v8
	v_fma_f32 v8, v68, v15, v20
	v_med3_f32 v8, v8, s73, v178
	v_add_f32_e32 v8, 1.0, v8
	v_mul_f32_e32 v16, v16, v17
	v_mul_f32_e32 v16, v8, v16
	v_add_f32_e32 v8, 1.0, v67
	v_rcp_f32_e32 v8, v8
	v_fma_f32 v17, v73, v15, v33
	v_med3_f32 v17, v17, s73, v178
	v_add_f32_e32 v17, 1.0, v17
	v_mul_f32_e32 v8, v66, v8
	v_mul_f32_e32 v17, v17, v8
	v_fma_f32 v8, v77, v15, v25
	v_min_f32_e32 v66, 0x40e00000, v8
	v_mul_f32_e32 v8, 0xc01d265f, v66
	v_exp_f32_e32 v8, v8
	v_fma_f32 v15, v69, v15, v21
	v_med3_f32 v15, v15, s73, v178
	s_waitcnt vmcnt(6)
	v_mul_f32_e32 v7, 0x3c800000, v7
	v_add_f32_e32 v8, 1.0, v8
	v_rcp_f32_e32 v67, v8
	v_mov_b32_e32 v8, 0
	v_cvt_pk_fp8_f32 v8, v9, v11
	v_mov_b32_e32 v9, 0
	v_cvt_pk_fp8_f32 v9, v10, v12
	v_add_u32_e32 v12, 0xa0, v5
	v_cvt_pk_fp8_f32 v8, v13, v17 op_sel:[0,0,1]
	v_add_u32_e32 v13, s50, v12
	v_cmp_lt_i32_e32 vcc, v13, v4
	v_add_f32_e32 v15, 1.0, v15
	v_mul_f32_e32 v10, v66, v67
	v_cndmask_b32_e32 v7, 0, v7, vcc
	v_mul_f32_e32 v10, v15, v10
	v_fma_f32 v13, v62, v7, v26
	v_cvt_pk_fp8_f32 v9, v16, v10 op_sel:[0,0,1]
	v_add_u32_e32 v10, s8, v14
	v_min_f32_e32 v13, 0x40e00000, v13
	v_ashrrev_i32_e32 v11, 31, v10
	v_mul_f32_e32 v14, 0xc01d265f, v13
	v_lshlrev_b64 v[10:11], 11, v[10:11]
	v_exp_f32_e32 v14, v14
	v_lshl_add_u64 v[10:11], s[26:27], 0, v[10:11]
	v_lshl_add_u64 v[10:11], v[10:11], 0, v[2:3]
	global_store_dwordx2 v[10:11], v[8:9], off
	v_fma_f32 v10, v58, v7, v22
	v_add_f32_e32 v8, 1.0, v14
	v_min_f32_e32 v10, 0x40e00000, v10
	v_rcp_f32_e32 v8, v8
	v_mul_f32_e32 v11, 0xc01d265f, v10
	v_exp_f32_e32 v11, v11
	v_fma_f32 v9, v54, v7, v30
	v_mul_f32_e32 v8, v13, v8
	v_fma_f32 v13, v63, v7, v27
	v_add_f32_e32 v11, 1.0, v11
	v_min_f32_e32 v13, 0x40e00000, v13
	v_med3_f32 v9, v9, s73, v178
	v_rcp_f32_e32 v11, v11
	v_mul_f32_e32 v14, 0xc01d265f, v13
	v_add_f32_e32 v9, 1.0, v9
	v_exp_f32_e32 v14, v14
	v_mul_f32_e32 v9, v9, v8
	v_fma_f32 v8, v50, v7, v18
	v_med3_f32 v8, v8, s73, v178
	v_add_f32_e32 v8, 1.0, v8
	v_mul_f32_e32 v10, v10, v11
	v_mul_f32_e32 v10, v8, v10
	v_add_f32_e32 v8, 1.0, v14
	v_rcp_f32_e32 v8, v8
	v_fma_f32 v15, v64, v7, v28
	v_fma_f32 v11, v55, v7, v31
	v_min_f32_e32 v15, 0x40e00000, v15
	v_mul_f32_e32 v8, v13, v8
	v_fma_f32 v13, v59, v7, v23
	v_min_f32_e32 v13, 0x40e00000, v13
	v_mul_f32_e32 v14, 0xc01d265f, v13
	v_exp_f32_e32 v14, v14
	v_med3_f32 v11, v11, s73, v178
	v_mul_f32_e32 v16, 0xc01d265f, v15
	v_add_f32_e32 v11, 1.0, v11
	v_add_f32_e32 v14, 1.0, v14
	v_rcp_f32_e32 v14, v14
	v_exp_f32_e32 v16, v16
	v_mul_f32_e32 v11, v11, v8
	v_fma_f32 v8, v51, v7, v19
	v_med3_f32 v8, v8, s73, v178
	v_add_f32_e32 v8, 1.0, v8
	v_mul_f32_e32 v13, v13, v14
	v_mul_f32_e32 v13, v8, v13
	v_add_f32_e32 v8, 1.0, v16
	v_rcp_f32_e32 v8, v8
	v_fma_f32 v17, v65, v7, v29
	v_fma_f32 v14, v56, v7, v32
	v_min_f32_e32 v17, 0x40e00000, v17
	v_mul_f32_e32 v8, v15, v8
	v_fma_f32 v15, v60, v7, v24
	v_min_f32_e32 v15, 0x40e00000, v15
	v_mul_f32_e32 v16, 0xc01d265f, v15
	v_exp_f32_e32 v16, v16
	v_med3_f32 v14, v14, s73, v178
	v_mul_f32_e32 v50, 0xc01d265f, v17
	v_add_f32_e32 v14, 1.0, v14
	v_add_f32_e32 v16, 1.0, v16
	v_rcp_f32_e32 v16, v16
	v_exp_f32_e32 v50, v50
	v_mul_f32_e32 v14, v14, v8
	v_fma_f32 v8, v52, v7, v20
	v_med3_f32 v8, v8, s73, v178
	v_add_f32_e32 v8, 1.0, v8
	v_mul_f32_e32 v15, v15, v16
	v_mul_f32_e32 v15, v8, v15
	v_add_f32_e32 v8, 1.0, v50
	v_rcp_f32_e32 v8, v8
	v_fma_f32 v16, v57, v7, v33
	v_med3_f32 v16, v16, s73, v178
	v_add_f32_e32 v16, 1.0, v16
	v_mul_f32_e32 v8, v17, v8
	v_mul_f32_e32 v16, v16, v8
	v_fma_f32 v8, v61, v7, v25
	v_min_f32_e32 v17, 0x40e00000, v8
	v_mul_f32_e32 v8, 0xc01d265f, v17
	v_exp_f32_e32 v8, v8
	v_fma_f32 v7, v53, v7, v21
	v_med3_f32 v7, v7, s73, v178
	v_add_f32_e32 v7, 1.0, v7
	v_add_f32_e32 v8, 1.0, v8
	v_rcp_f32_e32 v50, v8
	v_mov_b32_e32 v8, 0
	v_cvt_pk_fp8_f32 v8, v9, v11
	v_mov_b32_e32 v9, 0
	v_cvt_pk_fp8_f32 v9, v10, v13
	v_mul_f32_e32 v10, v17, v50
	v_mul_f32_e32 v7, v7, v10
	s_waitcnt vmcnt(6)
; __device__ __forceinline__ unsigned cvt4_fp8(float a, float b, float c, float d) { int w = 0; w = __builtin_amdgcn_cvt_pk_fp8_f32(a, b, w, false); w = __builtin_amdgcn_cvt_pk_fp8_f32(c, d, w, true); return (unsigned)w; }
; __device__ __forceinline__ float sig1702_(float x) { return __builtin_amdgcn_rcpf(1.0f + __builtin_amdgcn_exp2f(x * -2.4554669f)); }
; #define PG8_BAR __builtin_amdgcn_s_barrier()
; template <class Epi, class Sched, bool GATHER, bool ALIGN_EPI, bool SP2, bool FP8>
; __device__ __forceinline__ void gemm_phase(LAS unsigned char* lds, const Gemm g, const Sched& S, const Epi& E) {
;     ...
;         if (!has_next) break;
; #pragma unroll
;         for (int a = 0; a < 2; ++a)
; #pragma unroll
;             for (int b = 0; b < 2; ++b)
; #pragma unroll
;                 for (int m = 0; m < 4; ++m)
; #pragma unroll
;                     for (int n = 0; n < 2; ++n) acc[a][b][m][n] = (f32x4){0.f, 0.f, 0.f, 0.f};
;         cur = nxt; cA = nA; cB = nB; ++ui;
;         vA0 = nvA0; vA1 = nvA1;
;         if constexpr (ALIGN_EPI) { if (wr == 1) PG8_BAR; }
;     __device__ __forceinline__ void operator()(const f32x4 (&acc)[2][2][4][2], const pg8::Unit& u, const Pre& pre, int wr, int wc, int fr, int fq) const {
;     ...
;             for (int m = 0; m < 4; ++m) { const int rit = ai * 128 + wr * 64 + m * 16 + fr, p = u.r0 + rit; const float rs = (p < ce) ? rsv[ai * 4 + m] * 0.015625f : 0.f;
;                 f32x4 gt0 = acc[ai][0][m][0] * rs + g0, gt1 = acc[ai][0][m][1] * rs + g1, up0 = acc[ai][1][m][0] * rs + u0, up1 = acc[ai][1][m][1] * rs + u1;
;                 float o[8];
; #pragma unroll
;                 for (int j = 0; j < 4; ++j) { float gv = fminf(gt0[j], 7.0f), uv = fminf(fmaxf(up0[j], -7.0f), 7.0f); o[j] = (uv + 1.0f) * (gv * sig1702_(gv));
;                     gv = fminf(gt1[j], 7.0f); uv = fminf(fmaxf(up1[j], -7.0f), 7.0f); o[4 + j] = (uv + 1.0f) * (gv * sig1702_(gv)); }
;                 u32x2 w; w.x = cvt4_fp8(o[0], o[1], o[2], o[3]); w.y = cvt4_fp8(o[4], o[5], o[6], o[7]);
;                 *(u32x2*)(ACT + (size_t)(u.pm * 256 + rit) * DFF + col) = w; }
	v_mul_f32_e32 v6, 0x3c800000, v6
	v_cvt_pk_fp8_f32 v9, v15, v7 op_sel:[0,0,1]
	v_add_u32_e32 v7, 0xb0, v5
	v_add_u32_e32 v5, s50, v7
	v_cmp_lt_i32_e32 vcc, v5, v4
	v_add_u32_e32 v10, s8, v12
	v_cvt_pk_fp8_f32 v8, v14, v16 op_sel:[0,0,1]
	v_cndmask_b32_e32 v6, 0, v6, vcc
	v_fma_f32 v4, v46, v6, v26
	v_ashrrev_i32_e32 v11, 31, v10
	v_min_f32_e32 v12, 0x40e00000, v4
	v_lshlrev_b64 v[10:11], 11, v[10:11]
	v_mul_f32_e32 v4, 0xc01d265f, v12
	v_exp_f32_e32 v13, v4
	v_lshl_add_u64 v[4:5], s[26:27], 0, v[10:11]
	v_lshl_add_u64 v[4:5], v[4:5], 0, v[2:3]
	global_store_dwordx2 v[4:5], v[8:9], off
	v_fma_f32 v8, v42, v6, v22
	v_min_f32_e32 v8, 0x40e00000, v8
	v_mul_f32_e32 v9, 0xc01d265f, v8
	v_exp_f32_e32 v9, v9
	v_add_f32_e32 v4, 1.0, v13
	v_rcp_f32_e32 v4, v4
	v_fma_f32 v10, v47, v6, v27
	v_fma_f32 v5, v38, v6, v30
	v_add_f32_e32 v9, 1.0, v9
	v_min_f32_e32 v10, 0x40e00000, v10
	v_med3_f32 v5, v5, s73, v178
	v_rcp_f32_e32 v9, v9
	v_mul_f32_e32 v11, 0xc01d265f, v10
	v_add_f32_e32 v5, 1.0, v5
	v_mul_f32_e32 v4, v12, v4
	v_exp_f32_e32 v11, v11
	v_mul_f32_e32 v5, v5, v4
	v_fma_f32 v4, v34, v6, v18
	v_med3_f32 v4, v4, s73, v178
	v_add_f32_e32 v4, 1.0, v4
	v_mul_f32_e32 v8, v8, v9
	v_mul_f32_e32 v8, v4, v8
	v_add_f32_e32 v4, 1.0, v11
	v_rcp_f32_e32 v4, v4
	v_fma_f32 v12, v48, v6, v28
	v_fma_f32 v9, v39, v6, v31
	v_min_f32_e32 v12, 0x40e00000, v12
	v_mul_f32_e32 v4, v10, v4
	v_fma_f32 v10, v43, v6, v23
	v_min_f32_e32 v10, 0x40e00000, v10
	v_mul_f32_e32 v11, 0xc01d265f, v10
	v_exp_f32_e32 v11, v11
	v_med3_f32 v9, v9, s73, v178
	v_mul_f32_e32 v13, 0xc01d265f, v12
	v_add_f32_e32 v9, 1.0, v9
	v_add_f32_e32 v11, 1.0, v11
	v_rcp_f32_e32 v11, v11
	v_exp_f32_e32 v13, v13
	v_mul_f32_e32 v9, v9, v4
	v_fma_f32 v4, v35, v6, v19
	v_med3_f32 v4, v4, s73, v178
	v_add_f32_e32 v4, 1.0, v4
	v_mul_f32_e32 v10, v10, v11
	v_mul_f32_e32 v10, v4, v10
	v_add_f32_e32 v4, 1.0, v13
	v_rcp_f32_e32 v4, v4
	v_fma_f32 v14, v49, v6, v29
	v_fma_f32 v11, v40, v6, v32
	v_min_f32_e32 v14, 0x40e00000, v14
	v_mul_f32_e32 v4, v12, v4
	v_fma_f32 v12, v44, v6, v24
	v_min_f32_e32 v12, 0x40e00000, v12
	v_mul_f32_e32 v13, 0xc01d265f, v12
	v_exp_f32_e32 v13, v13
	v_med3_f32 v11, v11, s73, v178
	v_mul_f32_e32 v15, 0xc01d265f, v14
	v_add_f32_e32 v11, 1.0, v11
	v_add_f32_e32 v13, 1.0, v13
	v_rcp_f32_e32 v13, v13
	v_exp_f32_e32 v15, v15
	v_mul_f32_e32 v11, v11, v4
	v_fma_f32 v4, v36, v6, v20
	v_med3_f32 v4, v4, s73, v178
	v_add_f32_e32 v4, 1.0, v4
	v_mul_f32_e32 v12, v12, v13
	v_mul_f32_e32 v12, v4, v12
	v_add_f32_e32 v4, 1.0, v15
	v_rcp_f32_e32 v4, v4
	v_fma_f32 v13, v41, v6, v33
	v_med3_f32 v13, v13, s73, v178
	v_add_f32_e32 v13, 1.0, v13
	v_mul_f32_e32 v4, v14, v4
	v_mul_f32_e32 v13, v13, v4
	v_fma_f32 v4, v45, v6, v25
	v_min_f32_e32 v14, 0x40e00000, v4
	v_mul_f32_e32 v4, 0xc01d265f, v14
	v_exp_f32_e32 v4, v4
	v_fma_f32 v6, v37, v6, v21
	v_med3_f32 v6, v6, s73, v178
	v_add_f32_e32 v6, 1.0, v6
	v_add_f32_e32 v4, 1.0, v4
	v_rcp_f32_e32 v15, v4
	v_mov_b32_e32 v4, 0
	v_cvt_pk_fp8_f32 v4, v5, v9
	v_mov_b32_e32 v5, 0
	v_cvt_pk_fp8_f32 v5, v8, v10
	v_mul_f32_e32 v8, v14, v15
	v_mul_f32_e32 v6, v6, v8
	v_cvt_pk_fp8_f32 v4, v11, v13 op_sel:[0,0,1]
	v_cvt_pk_fp8_f32 v5, v12, v6 op_sel:[0,0,1]
	v_add_u32_e32 v6, s8, v7
	v_ashrrev_i32_e32 v7, 31, v6
	v_lshlrev_b64 v[6:7], 11, v[6:7]
	v_lshl_add_u64 v[6:7], s[26:27], 0, v[6:7]
	v_lshl_add_u64 v[2:3], v[6:7], 0, v[2:3]
	s_and_b64 vcc, exec, s[0:1]
	s_mov_b64 s[0:1], -1
	global_store_dwordx2 v[2:3], v[4:5], off
	s_cbranch_vccnz .LBB0_925
	s_andn2_b64 vcc, exec, s[54:55]
	s_cbranch_vccnz .LBB0_924
	s_barrier
	s_branch .LBB0_924

; __global__ void __launch_bounds__(512, 2) hymba_fwd(Params p) {
	.amdhsa_kernel _Z9hymba_fwd6Params
		.amdhsa_group_segment_fixed_size 0
		.amdhsa_private_segment_fixed_size 0
		.amdhsa_kernarg_size 456
		.amdhsa_user_sgpr_count 2
		.amdhsa_user_sgpr_dispatch_ptr 0
		.amdhsa_user_sgpr_queue_ptr 0
		.amdhsa_user_sgpr_kernarg_segment_ptr 1
		.amdhsa_user_sgpr_dispatch_id 0
		.amdhsa_user_sgpr_kernarg_preload_length 0
		.amdhsa_user_sgpr_kernarg_preload_offset 0
		.amdhsa_user_sgpr_private_segment_size 0
		.amdhsa_uses_dynamic_stack 0
		.amdhsa_enable_private_segment 0
		.amdhsa_system_sgpr_workgroup_id_x 1
		.amdhsa_system_sgpr_workgroup_id_y 0
		.amdhsa_system_sgpr_workgroup_id_z 0
		.amdhsa_system_sgpr_workgroup_info 0
		.amdhsa_system_vgpr_workitem_id 0
		.amdhsa_next_free_vgpr 248
		.amdhsa_next_free_sgpr 102
		.amdhsa_accum_offset 248
		.amdhsa_reserve_vcc 1
		.amdhsa_float_round_mode_32 0
		.amdhsa_float_round_mode_16_64 0
		.amdhsa_float_denorm_mode_32 3
		.amdhsa_float_denorm_mode_16_64 3
		.amdhsa_dx10_clamp 1
		.amdhsa_ieee_mode 1
		.amdhsa_fp16_overflow 0
		.amdhsa_tg_split 0
		.amdhsa_exception_fp_ieee_invalid_op 0
		.amdhsa_exception_fp_denorm_src 0
		.amdhsa_exception_fp_ieee_div_zero 0
		.amdhsa_exception_fp_ieee_overflow 0
		.amdhsa_exception_fp_ieee_underflow 0
		.amdhsa_exception_fp_ieee_inexact 0
		.amdhsa_exception_int_div_zero 0
	.end_amdhsa_kernel

; __global__ void __launch_bounds__(512, 2) hymba_fwd(Params p) {
amdhsa.kernels:
  - .agpr_count:     0
    .args:
      - .offset:         0
        .size:           200
        .value_kind:     by_value
      - .offset:         200
        .size:           4
        .value_kind:     hidden_block_count_x
      - .offset:         204
        .size:           4
        .value_kind:     hidden_block_count_y
      - .offset:         208
        .size:           4
        .value_kind:     hidden_block_count_z
      - .offset:         212
        .size:           2
        .value_kind:     hidden_group_size_x
      - .offset:         214
        .size:           2
        .value_kind:     hidden_group_size_y
      - .offset:         216
        .size:           2
        .value_kind:     hidden_group_size_z
      - .offset:         218
        .size:           2
        .value_kind:     hidden_remainder_x
      - .offset:         220
        .size:           2
        .value_kind:     hidden_remainder_y
      - .offset:         222
        .size:           2
        .value_kind:     hidden_remainder_z
      - .offset:         240
        .size:           8
        .value_kind:     hidden_global_offset_x
      - .offset:         248
        .size:           8
        .value_kind:     hidden_global_offset_y
      - .offset:         256
        .size:           8
        .value_kind:     hidden_global_offset_z
      - .offset:         264
        .size:           2
        .value_kind:     hidden_grid_dims
      - .offset:         320
        .size:           4
        .value_kind:     hidden_dynamic_lds_size
    .group_segment_fixed_size: 0
    .kernarg_segment_align: 8
    .kernarg_segment_size: 456
    .language:       OpenCL C
    .language_version:
      - 2
      - 0
    .max_flat_workgroup_size: 512
    .name:           _Z9hymba_fwd6Params
    .private_segment_fixed_size: 0
    .sgpr_count:     108
    .sgpr_spill_count: 132
    .symbol:         _Z9hymba_fwd6Params.kd
    .uniform_work_group_size: 1
    .uses_dynamic_stack: false
    .vgpr_count:     248
    .vgpr_spill_count: 0
    .wavefront_size: 64
